# prologue: nt (streaming) cache policy on the once-read f32 weight and x loads
# speedup vs baseline: 1.0126x; 1.0010x over previous
.LBB0_64:
	s_lshr_b32 s24, s4, 7
	s_waitcnt vmcnt(0)
	v_cvt_f32_u32_e32 v0, s24
	s_sub_i32 s25, 0, s24
	s_xor_b64 s[34:35], s[2:3], -1
	s_ashr_i32 s2, s58, 2
	v_rcp_iflag_f32_e32 v0, v0
	s_abs_i32 s3, s2
	v_mul_f32_e32 v0, 0x4f7ffffe, v0
	v_cvt_u32_f32_e32 v0, v0
	s_nop 0
	v_readfirstlane_b32 s36, v0
	s_mul_i32 s25, s25, s36
	s_mul_hi_u32 s25, s36, s25
	s_add_i32 s36, s36, s25
	s_mul_hi_u32 s25, s3, s36
	s_mul_i32 s36, s25, s24
	s_sub_i32 s3, s3, s36
	s_add_i32 s37, s25, 1
	s_sub_i32 s36, s3, s24
	s_cmp_ge_u32 s3, s24
	s_cselect_b32 s25, s37, s25
	s_cselect_b32 s3, s36, s3
	s_add_i32 s36, s25, 1
	s_cmp_ge_u32 s3, s24
	s_cselect_b32 s3, s36, s25
	s_ashr_i32 s59, s58, 31
	s_xor_b32 s3, s3, s59
	s_sub_i32 s3, s3, s59
	s_mul_i32 s24, s3, s24
	s_lshl_b32 s3, s3, 6
	v_or_b32_e32 v0, s3, v136
	s_ashr_i32 s3, s3, 31
	s_sub_i32 s2, s2, s24
	s_mul_i32 s3, s3, s4
	v_mad_u64_u32 v[0:1], s[24:25], v0, s4, 0
	s_lshl_b32 s2, s2, 7
	v_add_u32_e32 v1, s3, v1
	s_waitcnt lgkmcnt(0)
	v_lshl_add_u64 v[0:1], v[0:1], 2, s[0:1]
	s_ashr_i32 s3, s2, 31
	v_lshl_add_u64 v[0:1], s[2:3], 2, v[0:1]
	v_lshl_add_u64 v[0:1], v[0:1], 0, v[142:143]
	s_lshl_b64 s[0:1], s[4:5], 5
	v_lshl_add_u64 v[2:3], v[0:1], 0, s[0:1]
	v_lshl_add_u64 v[4:5], v[2:3], 0, s[0:1]
	global_load_dwordx4 v[120:123], v[2:3], off nt
	global_load_dwordx4 v[116:119], v[4:5], off nt
	v_lshl_add_u64 v[2:3], v[4:5], 0, s[0:1]
	v_lshl_add_u64 v[4:5], v[2:3], 0, s[0:1]
	global_load_dwordx4 v[108:111], v[2:3], off nt
	global_load_dwordx4 v[100:103], v[4:5], off nt
	v_lshl_add_u64 v[2:3], v[4:5], 0, s[0:1]
	v_lshl_add_u64 v[4:5], v[2:3], 0, s[0:1]
	v_lshl_add_u64 v[6:7], v[4:5], 0, s[0:1]
	v_mad_u64_u32 v[8:9], s[2:3], s4, v164, v[6:7]
	v_subrev_u32_e32 v9, s4, v9
	v_lshl_add_u64 v[10:11], v[8:9], 0, s[0:1]
	v_lshl_add_u64 v[12:13], v[10:11], 0, s[0:1]
	v_lshl_add_u64 v[14:15], v[12:13], 0, s[0:1]
	v_lshl_add_u64 v[16:17], v[14:15], 0, s[0:1]
	v_lshl_add_u64 v[18:19], v[16:17], 0, s[0:1]
	v_lshl_add_u64 v[20:21], v[18:19], 0, s[0:1]
	v_mad_u64_u32 v[22:23], s[2:3], s4, v164, v[20:21]
	v_subrev_u32_e32 v23, s4, v23
	v_lshl_add_u64 v[24:25], v[22:23], 0, s[0:1]
	v_lshl_add_u64 v[26:27], v[24:25], 0, s[0:1]
	v_lshl_add_u64 v[28:29], v[26:27], 0, s[0:1]
	v_lshl_add_u64 v[30:31], v[28:29], 0, s[0:1]
	v_lshl_add_u64 v[32:33], v[30:31], 0, s[0:1]
	v_lshl_add_u64 v[34:35], v[32:33], 0, s[0:1]
	v_mad_u64_u32 v[128:129], s[2:3], s4, v164, v[34:35]
	global_load_dwordx4 v[112:115], v[2:3], off nt
	global_load_dwordx4 v[104:107], v[4:5], off nt
	global_load_dwordx4 v[96:99], v[6:7], off nt
	global_load_dwordx4 v[88:91], v[8:9], off offset:128 nt
	global_load_dwordx4 v[84:87], v[10:11], off offset:128 nt
	global_load_dwordx4 v[80:83], v[12:13], off offset:128 nt
	global_load_dwordx4 v[76:79], v[14:15], off offset:128 nt
	global_load_dwordx4 v[72:75], v[16:17], off offset:128 nt
	global_load_dwordx4 v[68:71], v[18:19], off offset:128 nt
	global_load_dwordx4 v[64:67], v[20:21], off offset:128 nt
	global_load_dwordx4 v[56:59], v[22:23], off offset:256 nt
	global_load_dwordx4 v[52:55], v[24:25], off offset:256 nt
	global_load_dwordx4 v[48:51], v[26:27], off offset:256 nt
	global_load_dwordx4 v[44:47], v[28:29], off offset:256 nt
	global_load_dwordx4 v[40:43], v[30:31], off offset:256 nt
	global_load_dwordx4 v[36:39], v[32:33], off offset:256 nt
	s_nop 0
	global_load_dwordx4 v[32:35], v[34:35], off offset:256 nt
	s_nop 0
	global_load_dwordx4 v[124:127], v[0:1], off nt
	global_load_dwordx4 v[92:95], v[0:1], off offset:128 nt
	global_load_dwordx4 v[60:63], v[0:1], off offset:256 nt
	global_load_dwordx4 v[28:31], v[0:1], off offset:384 nt
	v_subrev_u32_e32 v129, s4, v129
	v_lshl_add_u64 v[0:1], v[128:129], 0, s[0:1]
	v_lshl_add_u64 v[2:3], v[0:1], 0, s[0:1]
	global_load_dwordx4 v[20:23], v[0:1], off offset:384 nt
	v_lshl_add_u64 v[0:1], v[2:3], 0, s[0:1]
	global_load_dwordx4 v[16:19], v[2:3], off offset:384 nt
	v_lshl_add_u64 v[2:3], v[0:1], 0, s[0:1]
	global_load_dwordx4 v[12:15], v[0:1], off offset:384 nt
	v_lshl_add_u64 v[0:1], v[2:3], 0, s[0:1]
	global_load_dwordx4 v[8:11], v[2:3], off offset:384 nt
	v_lshl_add_u64 v[2:3], v[0:1], 0, s[0:1]
	global_load_dwordx4 v[24:27], v[128:129], off offset:384 nt
	global_load_dwordx4 v[4:7], v[0:1], off offset:384 nt
	s_nop 0
	global_load_dwordx4 v[0:3], v[2:3], off offset:384 nt
	s_lshr_b32 s4, s4, 5
	v_cvt_f32_u32_e32 v128, s4
	s_sub_i32 s3, 0, s4
	s_abs_i32 s2, s58
	s_mov_b64 s[0:1], -1
	v_rcp_iflag_f32_e32 v128, v128
	s_nop 0
	v_mul_f32_e32 v128, 0x4f7ffffe, v128
	v_cvt_u32_f32_e32 v128, v128
	s_nop 0
	v_readfirstlane_b32 s56, v128
	s_mul_i32 s3, s3, s56
	s_mul_hi_u32 s3, s56, s3
	s_add_i32 s56, s56, s3
	s_mul_hi_u32 s3, s2, s56
	s_mul_i32 s24, s3, s4
	s_sub_i32 s60, s2, s24
	s_add_i32 s2, s3, 1
	s_sub_i32 s61, s60, s4
	s_cmp_ge_u32 s60, s4
	s_cselect_b32 s2, s2, s3
	s_cselect_b32 s3, s61, s60
	s_add_i32 s24, s2, 1
	s_cmp_ge_u32 s3, s4
	s_cselect_b32 s2, s24, s2
	s_xor_b32 s2, s2, s59
	s_sub_i32 s38, s2, s59
	s_lshl_b32 s36, s38, 6
	s_cmp_lg_u64 s[22:23], 0
	s_cselect_b64 s[24:25], -1, 0
	s_and_b64 vcc, exec, s[34:35]
	s_cbranch_vccz .LBB0_125
	s_cmp_lt_i32 s57, 1
	s_cbranch_scc1 .LBB0_110
	s_cmp_lt_i32 s57, 2
	s_cbranch_scc1 .LBB0_95
	s_cmp_lg_u32 s57, 2
	s_cbranch_scc0 .LBB0_81
	v_cndmask_b32_e64 v128, 0, 1, s[24:25]
	v_cmp_ne_u32_e64 s[2:3], 1, v128
	s_andn2_b64 vcc, exec, s[24:25]
	s_cbranch_vccnz .LBB0_854
	v_or_b32_e32 v128, s36, v136
	s_ashr_i32 s37, s36, 31
	v_ashrrev_i32_e32 v129, 31, v128
	v_lshl_add_u64 v[130:131], s[36:37], 0, v[136:137]
	v_lshl_add_u64 v[128:129], v[128:129], 2, s[22:23]
	v_lshl_add_u64 v[130:131], v[130:131], 2, s[22:23]
	global_load_dword v128, v[128:129], off
	s_nop 0
	global_load_dword v132, v[130:131], off offset:32
	s_waitcnt vmcnt(1)
	v_pk_mul_f32 v[134:135], v[126:127], v[128:129] op_sel_hi:[1,0]
	v_pk_mul_f32 v[168:169], v[124:125], v[128:129] op_sel_hi:[1,0]
	s_waitcnt vmcnt(0)
	v_pk_mul_f32 v[130:131], v[122:123], v[132:133] op_sel_hi:[1,0]
	v_pk_mul_f32 v[128:129], v[120:121], v[132:133] op_sel_hi:[1,0]
	ds_write2_b32 v145, v168, v169 offset1:1
	ds_write2_b32 v145, v134, v135 offset0:2 offset1:3
	s_cbranch_execnz .LBB0_71

.LBB0_911:
	s_mov_b32 s4, 0
	s_ashr_i32 s5, s4, 31
	s_lshl_b64 s[4:5], s[4:5], 3
	s_add_u32 s4, s92, s4
	s_addc_u32 s5, s93, s5
	s_load_dwordx2 s[4:5], s[4:5], 0x0
	s_waitcnt lgkmcnt(0)
	v_lshl_add_u64 v[8:9], s[6:7], 0, v[4:5]
	v_lshl_add_u64 v[42:43], s[4:5], 0, v[2:3]
	global_load_dwordx4 v[14:17], v[42:43], off offset:-4096 nt
	global_load_dwordx4 v[18:21], v[42:43], off offset:-3072 nt
	global_load_dwordx4 v[22:25], v[42:43], off offset:-2048 nt
	global_load_dwordx4 v[26:29], v[42:43], off offset:-1024 nt
	global_load_dwordx4 v[30:33], v[42:43], off nt
	global_load_dwordx4 v[34:37], v[42:43], off offset:1024 nt
	global_load_dwordx4 v[38:41], v[42:43], off offset:2048 nt
	s_nop 0
	global_load_dwordx4 v[42:45], v[42:43], off offset:3072 nt
	v_add_co_u32_e64 v8, s[4:5], s9, v8
	v_lshl_add_u64 v[10:11], s[6:7], 0, v[6:7]
	s_nop 0
	v_addc_co_u32_e64 v9, s[4:5], 0, v9, s[4:5]
	v_add_co_u32_e64 v10, s[4:5], s11, v10
	s_nop 1
	v_addc_co_u32_e64 v11, s[4:5], 0, v11, s[4:5]
	s_waitcnt vmcnt(7)
	v_mul_f32_e32 v46, v15, v15
	v_mul_f32_e32 v13, v17, v17
	v_fmac_f32_e32 v46, v14, v14
	v_fmac_f32_e32 v13, v16, v16
	v_add_f32_e32 v46, v46, v13
	v_cvt_pk_fp8_f32 v13, v14, v15
	v_cvt_pk_fp8_f32 v13, v16, v17 op_sel:[0,0,1]
	global_store_dword v[10:11], v13, off
	v_cvt_pk_bf16_f32 v14, v14, v15
	v_cvt_pk_bf16_f32 v15, v16, v17
	global_store_dwordx2 v[8:9], v[14:15], off
	s_waitcnt vmcnt(8)
	v_mul_f32_e32 v13, v19, v19
	v_mul_f32_e32 v16, v21, v21
	v_fmac_f32_e32 v13, v18, v18
	v_fmac_f32_e32 v16, v20, v20
	v_add_f32_e32 v13, v13, v16
	v_add_f32_e32 v46, v46, v13
	v_cvt_pk_fp8_f32 v13, v18, v19
	v_cvt_pk_fp8_f32 v13, v20, v21 op_sel:[0,0,1]
	global_store_dword v[10:11], v13, off offset:256
	v_cvt_pk_bf16_f32 v18, v18, v19
	v_cvt_pk_bf16_f32 v19, v20, v21
	global_store_dwordx2 v[8:9], v[18:19], off offset:512
	s_waitcnt vmcnt(9)
	v_mul_f32_e32 v13, v23, v23
	v_mul_f32_e32 v20, v25, v25
	v_fmac_f32_e32 v13, v22, v22
	v_fmac_f32_e32 v20, v24, v24
	v_add_f32_e32 v13, v13, v20
	v_add_f32_e32 v46, v46, v13
	v_cvt_pk_fp8_f32 v13, v22, v23
	v_cvt_pk_fp8_f32 v13, v24, v25 op_sel:[0,0,1]
	global_store_dword v[10:11], v13, off offset:512
	v_cvt_pk_bf16_f32 v22, v22, v23
	v_cvt_pk_bf16_f32 v23, v24, v25
	global_store_dwordx2 v[8:9], v[22:23], off offset:1024
	s_waitcnt vmcnt(10)
	v_mul_f32_e32 v13, v27, v27
	v_mul_f32_e32 v24, v29, v29
	v_fmac_f32_e32 v13, v26, v26
	v_fmac_f32_e32 v24, v28, v28
	v_add_f32_e32 v13, v13, v24
	v_add_f32_e32 v46, v46, v13
	v_cvt_pk_fp8_f32 v13, v26, v27
	v_cvt_pk_fp8_f32 v13, v28, v29 op_sel:[0,0,1]
	global_store_dword v[10:11], v13, off offset:768
	v_cvt_pk_bf16_f32 v26, v26, v27
	v_cvt_pk_bf16_f32 v27, v28, v29
	global_store_dwordx2 v[8:9], v[26:27], off offset:1536
	s_waitcnt vmcnt(11)
	v_mul_f32_e32 v13, v31, v31
	v_mul_f32_e32 v28, v33, v33
	v_fmac_f32_e32 v13, v30, v30
	v_fmac_f32_e32 v28, v32, v32
	v_add_f32_e32 v13, v13, v28
	v_add_f32_e32 v46, v46, v13
	v_cvt_pk_fp8_f32 v13, v30, v31
	v_cvt_pk_fp8_f32 v13, v32, v33 op_sel:[0,0,1]
	global_store_dword v[10:11], v13, off offset:1024
	v_cvt_pk_bf16_f32 v30, v30, v31
	v_cvt_pk_bf16_f32 v31, v32, v33
	global_store_dwordx2 v[8:9], v[30:31], off offset:2048
	s_waitcnt vmcnt(12)
	v_mul_f32_e32 v13, v35, v35
	v_mul_f32_e32 v32, v37, v37
	v_fmac_f32_e32 v13, v34, v34
	v_fmac_f32_e32 v32, v36, v36
	v_add_f32_e32 v13, v13, v32
	v_add_f32_e32 v46, v46, v13
	v_cvt_pk_fp8_f32 v13, v34, v35
	v_cvt_pk_fp8_f32 v13, v36, v37 op_sel:[0,0,1]
	global_store_dword v[10:11], v13, off offset:1280
	v_cvt_pk_bf16_f32 v34, v34, v35
	v_cvt_pk_bf16_f32 v35, v36, v37
	global_store_dwordx2 v[8:9], v[34:35], off offset:2560
	s_waitcnt vmcnt(13)
	v_mul_f32_e32 v13, v39, v39
	v_mul_f32_e32 v36, v41, v41
	v_fmac_f32_e32 v13, v38, v38
	v_fmac_f32_e32 v36, v40, v40
	v_add_f32_e32 v13, v13, v36
	v_add_f32_e32 v46, v46, v13
	v_cvt_pk_fp8_f32 v13, v38, v39
	v_cvt_pk_fp8_f32 v13, v40, v41 op_sel:[0,0,1]
	global_store_dword v[10:11], v13, off offset:1536
	v_cvt_pk_bf16_f32 v38, v38, v39
	v_cvt_pk_bf16_f32 v39, v40, v41
	global_store_dwordx2 v[8:9], v[38:39], off offset:3072
	s_waitcnt vmcnt(14)
	v_mul_f32_e32 v13, v43, v43
	v_mul_f32_e32 v40, v45, v45
	v_fmac_f32_e32 v13, v42, v42
	v_fmac_f32_e32 v40, v44, v44
	v_add_f32_e32 v13, v13, v40
	v_add_f32_e32 v46, v46, v13
	v_cvt_pk_fp8_f32 v13, v42, v43
	v_cvt_pk_fp8_f32 v13, v44, v45 op_sel:[0,0,1]
	global_store_dword v[10:11], v13, off offset:1792
	v_cvt_pk_bf16_f32 v42, v42, v43
	v_cvt_pk_bf16_f32 v43, v44, v45
	global_store_dwordx2 v[8:9], v[42:43], off offset:3584
	v_mov_b32_e32 v9, v46
	v_mbcnt_lo_u32_b32 v8, -1, 0
	v_mbcnt_hi_u32_b32 v8, -1, v8
	v_mbcnt_lo_u32_b32 v10, -1, 0
	v_mbcnt_hi_u32_b32 v10, -1, v10
	s_nop 0
	v_lshlrev_b32_e32 v8, 2, v8
	v_xor_b32_e32 v8, 4, v8
	ds_bpermute_b32 v8, v8, v9
	v_lshlrev_b32_e32 v10, 2, v10
	v_xor_b32_e32 v10, 8, v10
	s_waitcnt lgkmcnt(0)
	v_add_f32_e32 v8, v9, v8
	ds_bpermute_b32 v9, v10, v8
	v_mbcnt_lo_u32_b32 v10, -1, 0
	v_mbcnt_hi_u32_b32 v10, -1, v10
	s_waitcnt lgkmcnt(0)
	v_add_f32_e32 v8, v8, v9
	v_lshlrev_b32_e32 v10, 2, v10
	v_xor_b32_e32 v10, 16, v10
	ds_bpermute_b32 v9, v10, v8
	v_mbcnt_lo_u32_b32 v10, -1, 0
	v_mbcnt_hi_u32_b32 v10, -1, v10
	s_waitcnt lgkmcnt(0)
	v_add_f32_e32 v8, v8, v9
	v_lshlrev_b32_e32 v10, 2, v10
	v_xor_b32_e32 v10, 32, v10
	ds_bpermute_b32 v9, v10, v8
	v_mbcnt_lo_u32_b32 v10, -1, 0
	v_mbcnt_hi_u32_b32 v10, -1, v10
	s_waitcnt lgkmcnt(0)
	v_add_f32_e32 v8, v8, v9
	v_lshlrev_b32_e32 v10, 2, v10
	v_xor_b32_e32 v10, 64, v10
	ds_bpermute_b32 v9, v10, v8
	v_mbcnt_lo_u32_b32 v10, -1, 0
	v_mbcnt_hi_u32_b32 v10, -1, v10
	s_waitcnt lgkmcnt(0)
	v_add_f32_e32 v8, v8, v9
	v_lshlrev_b32_e32 v10, 2, v10
	v_xor_b32_e32 v9, 0x80, v10
	ds_bpermute_b32 v9, v9, v8
	s_and_saveexec_b64 s[4:5], vcc
	s_cbranch_execz .LBB0_910
	s_waitcnt lgkmcnt(0)
	v_add_f32_e32 v8, v8, v9
	v_lshl_add_u64 v[10:11], s[6:7], 0, v[0:1]
	v_cndmask_b32_e64 v8, 0, v8, s[2:3]
	global_store_dword v[10:11], v8, off
	s_branch .LBB0_910
